# v61 + fp8 in-proj rope epilogue: rope-table loads of row groups issued two groups ahead into spare/consumed registers, counted waits
# speedup vs baseline: 1.0059x; 1.0059x over previous
.LBB0_3481:
	s_and_b64 s[4:5], s[6:7], exec
	s_cselect_b32 s4, s94, 0
	v_or_b32_e32 v66, s4, v250
	s_mov_b32 s4, 0x14e00000
	s_cselect_b32 s4, s4, 0x15600000
	s_add_u32 s84, s8, s4
	s_addc_u32 s85, s9, 0
	s_and_b64 s[4:5], s[6:7], exec
	v_lshlrev_b32_e32 v68, 3, v66
	v_mov_b32_e32 v69, v1
	v_cndmask_b32_e64 v19, 0, 1, s[62:63]
	s_cselect_b32 s64, 6, 5
	v_cmp_ne_u32_e64 s[4:5], 1, v19
	s_andn2_b64 vcc, exec, s[62:63]
	v_lshl_add_u64 v[68:69], s[84:85], 0, v[68:69]
	s_cbranch_vccnz .LBB0_3483
	v_ashrrev_i32_e32 v19, 31, v18
	v_lshlrev_b64 v[70:71], s64, v[18:19]
	v_lshl_add_u64 v[70:71], v[70:71], 3, v[68:69]
	global_load_dwordx4 v[92:95], v[70:71], off offset:48
	global_load_dwordx4 v[72:75], v[70:71], off offset:32
	global_load_dwordx4 v[76:79], v[70:71], off offset:16
	global_load_dwordx4 v[80:83], v[70:71], off
	v_add_u32_e32 v128, 0x10, v18
	v_ashrrev_i32_e32 v129, 31, v128
	v_lshlrev_b64 v[128:129], s64, v[128:129]
	v_lshl_add_u64 v[128:129], v[128:129], 3, v[68:69]
	global_load_dwordx4 v[106:109], v[128:129], off offset:48
	global_load_dwordx4 v[110:113], v[128:129], off offset:32
	global_load_dwordx4 v[114:117], v[128:129], off offset:16
	global_load_dwordx4 v[118:121], v[128:129], off
	s_waitcnt vmcnt(4)
	v_mul_f32_e32 v98, v188, v92
	v_mov_b32_e32 v87, v74
	v_mov_b32_e32 v74, v73
	v_mov_b32_e32 v71, v82
	v_mov_b32_e32 v82, v81
	v_mov_b32_e32 v70, v80
	v_pk_mul_f32 v[96:97], v[158:159], v[82:83]
	v_pk_mul_f32 v[80:81], v[190:191], v[82:83]
	v_mov_b32_e32 v83, v78
	v_mov_b32_e32 v78, v77
	v_mov_b32_e32 v82, v76
	v_pk_mul_f32 v[76:77], v[160:161], v[78:79]
	v_pk_mul_f32 v[84:85], v[192:193], v[78:79]
	v_mov_b32_e32 v86, v72
	v_pk_mul_f32 v[72:73], v[154:155], v[74:75]
	v_pk_mul_f32 v[88:89], v[186:187], v[74:75]
	v_mov_b32_e32 v74, v189
	v_mov_b32_e32 v75, v157
	v_pk_fma_f32 v[78:79], v[190:191], v[70:71], v[96:97] neg_lo:[0,0,1] neg_hi:[0,0,1]
	v_mov_b32_e32 v96, v157
	v_mov_b32_e32 v97, v189
	v_pk_mul_f32 v[74:75], v[74:75], v[94:95]
	v_pk_mul_f32 v[94:95], v[96:97], v[94:95]
	v_mul_f32_e32 v100, v156, v93
	v_mul_f32_e32 v90, v156, v92
	v_mul_f32_e32 v92, v188, v93
	v_mov_b32_e32 v99, v74
	v_mov_b32_e32 v101, v75
	v_mov_b32_e32 v91, v94
	v_mov_b32_e32 v93, v95
	v_pk_fma_f32 v[76:77], v[192:193], v[82:83], v[76:77] neg_lo:[0,0,1] neg_hi:[0,0,1]
	v_pk_fma_f32 v[74:75], v[186:187], v[86:87], v[72:73] neg_lo:[0,0,1] neg_hi:[0,0,1]
	v_pk_add_f32 v[72:73], v[98:99], v[100:101] neg_lo:[0,1] neg_hi:[0,1]
	v_pk_fma_f32 v[94:95], v[158:159], v[70:71], v[80:81]
	v_pk_fma_f32 v[84:85], v[160:161], v[82:83], v[84:85]
	v_pk_fma_f32 v[82:83], v[154:155], v[86:87], v[88:89]
	v_pk_add_f32 v[80:81], v[90:91], v[92:93]
	v_add_u32_e32 v128, 0x20, v18
	v_ashrrev_i32_e32 v129, 31, v128
	v_lshlrev_b64 v[128:129], s64, v[128:129]
	v_lshl_add_u64 v[128:129], v[128:129], 3, v[68:69]
	global_load_dwordx4 v[154:157], v[128:129], off offset:48
	global_load_dwordx4 v[158:161], v[128:129], off offset:32
	global_load_dwordx4 v[186:189], v[128:129], off offset:16
	global_load_dwordx4 v[190:193], v[128:129], off
	s_branch .LBB0_3484

.LBB0_3488:
	v_pk_mul_f32 v[74:75], s[56:57], v[74:75] op_sel_hi:[0,1]
	v_pk_mul_f32 v[72:73], s[56:57], v[72:73] op_sel_hi:[0,1]
	v_pk_mul_f32 v[76:77], s[56:57], v[76:77] op_sel_hi:[0,1]
	v_cvt_pk_bf16_f32 v90, v74, v75
	v_cvt_pk_bf16_f32 v91, v72, v73
	v_pk_mul_f32 v[72:73], s[56:57], v[94:95] op_sel_hi:[0,1]
	v_pk_mul_f32 v[74:75], s[56:57], v[84:85] op_sel_hi:[0,1]
	s_and_b64 s[6:7], s[6:7], exec
	v_pk_mul_f32 v[78:79], s[56:57], v[78:79] op_sel_hi:[0,1]
	v_cvt_pk_bf16_f32 v89, v76, v77
	v_cvt_pk_bf16_f32 v72, v72, v73
	v_cvt_pk_bf16_f32 v73, v74, v75
	v_pk_mul_f32 v[74:75], s[56:57], v[82:83] op_sel_hi:[0,1]
	v_pk_mul_f32 v[76:77], s[56:57], v[80:81] op_sel_hi:[0,1]
	s_cselect_b32 s0, 64, 32
	v_cvt_pk_bf16_f32 v88, v78, v79
	v_cvt_pk_bf16_f32 v74, v74, v75
	v_cvt_pk_bf16_f32 v75, v76, v77
	v_lshl_add_u64 v[76:77], v[86:87], 1, s[54:55]
	s_lshl_b32 s92, s0, 1
	global_store_dwordx4 v[76:77], v[88:91], off
	v_lshl_add_u64 v[76:77], v[76:77], 0, s[92:93]
	global_store_dwordx4 v[76:77], v[72:75], off
	s_and_b64 vcc, exec, s[4:5]
	s_nop 0
	v_or_b32_e32 v72, 16, v18
	v_ashrrev_i32_e32 v73, 31, v72
	s_cbranch_vccnz .LBB0_3490
	v_lshlrev_b64 v[74:75], s64, v[72:73]
	v_lshl_add_u64 v[74:75], v[74:75], 3, v[68:69]
	v_mov_b32_e32 v94, v181
	v_mov_b32_e32 v95, v149
	s_waitcnt vmcnt(4)
	v_mov_b64_e32 v[96:97], v[106:107]
	v_mov_b64_e32 v[98:99], v[108:109]
	v_mov_b64_e32 v[84:85], v[110:111]
	v_mov_b64_e32 v[86:87], v[112:113]
	v_mov_b64_e32 v[80:81], v[114:115]
	v_mov_b64_e32 v[82:83], v[116:117]
	v_mov_b64_e32 v[76:77], v[118:119]
	v_mov_b64_e32 v[78:79], v[120:121]
	v_pk_mul_f32 v[94:95], v[94:95], v[98:99]
	v_mul_f32_e32 v100, v180, v96
	v_mul_f32_e32 v102, v148, v97
	v_mov_b32_e32 v75, v78
	v_mov_b32_e32 v78, v77
	v_mov_b32_e32 v74, v76
	v_pk_mul_f32 v[88:89], v[150:151], v[78:79]
	v_pk_mul_f32 v[76:77], v[182:183], v[78:79]
	v_mov_b32_e32 v79, v82
	v_mov_b32_e32 v82, v81
	v_mov_b32_e32 v78, v80
	v_pk_mul_f32 v[90:91], v[152:153], v[82:83]
	v_pk_mul_f32 v[80:81], v[184:185], v[82:83]
	v_mov_b32_e32 v83, v86
	v_mov_b32_e32 v86, v85
	v_mov_b32_e32 v82, v84
	v_pk_mul_f32 v[84:85], v[146:147], v[86:87]
	v_mov_b32_e32 v101, v94
	v_mov_b32_e32 v103, v95
	v_pk_fma_f32 v[94:95], v[182:183], v[74:75], v[88:89] neg_lo:[0,0,1] neg_hi:[0,0,1]
	v_pk_fma_f32 v[88:89], v[178:179], v[82:83], v[84:85] neg_lo:[0,0,1] neg_hi:[0,0,1]
	v_pk_add_f32 v[84:85], v[100:101], v[102:103] neg_lo:[0,1] neg_hi:[0,1]
	v_mov_b32_e32 v100, v149
	v_mov_b32_e32 v101, v181
	v_pk_mul_f32 v[98:99], v[100:101], v[98:99]
	v_pk_mul_f32 v[86:87], v[178:179], v[86:87]
	v_mul_f32_e32 v92, v148, v96
	v_mul_f32_e32 v96, v180, v97
	v_mov_b32_e32 v93, v98
	v_mov_b32_e32 v97, v99
	v_pk_fma_f32 v[90:91], v[184:185], v[78:79], v[90:91] neg_lo:[0,0,1] neg_hi:[0,0,1]
	v_pk_fma_f32 v[98:99], v[150:151], v[74:75], v[76:77]
	v_pk_fma_f32 v[78:79], v[152:153], v[78:79], v[80:81]
	v_pk_fma_f32 v[76:77], v[146:147], v[82:83], v[86:87]
	v_pk_add_f32 v[74:75], v[92:93], v[96:97]
	v_add_u32_e32 v128, 0x30, v18
	v_ashrrev_i32_e32 v129, 31, v128
	v_lshlrev_b64 v[128:129], s64, v[128:129]
	v_lshl_add_u64 v[128:129], v[128:129], 3, v[68:69]
	global_load_dwordx4 v[146:149], v[128:129], off offset:48
	global_load_dwordx4 v[150:153], v[128:129], off offset:32
	global_load_dwordx4 v[178:181], v[128:129], off offset:16
	global_load_dwordx4 v[182:185], v[128:129], off
	s_branch .LBB0_3491

.LBB0_3495:
	s_mov_b32 s57, s56
	v_pk_mul_f32 v[72:73], s[56:57], v[94:95]
	s_and_b64 vcc, exec, s[4:5]
	v_cvt_pk_bf16_f32 v86, v72, v73
	v_pk_mul_f32 v[72:73], s[56:57], v[90:91]
	s_nop 0
	v_cvt_pk_bf16_f32 v87, v72, v73
	v_pk_mul_f32 v[72:73], s[56:57], v[88:89]
	s_nop 0
	v_cvt_pk_bf16_f32 v88, v72, v73
	v_pk_mul_f32 v[72:73], s[56:57], v[84:85]
	s_nop 0
	v_cvt_pk_bf16_f32 v89, v72, v73
	v_pk_mul_f32 v[72:73], s[56:57], v[98:99]
	s_nop 0
	v_cvt_pk_bf16_f32 v82, v72, v73
	v_pk_mul_f32 v[72:73], s[56:57], v[78:79]
	s_nop 0
	v_cvt_pk_bf16_f32 v83, v72, v73
	v_pk_mul_f32 v[72:73], s[56:57], v[76:77]
	s_nop 0
	v_cvt_pk_bf16_f32 v84, v72, v73
	v_pk_mul_f32 v[72:73], s[56:57], v[74:75]
	s_nop 0
	v_cvt_pk_bf16_f32 v85, v72, v73
	v_lshl_add_u64 v[72:73], v[80:81], 1, s[54:55]
	global_store_dwordx4 v[72:73], v[86:89], off
	v_lshl_add_u64 v[72:73], v[72:73], 0, s[92:93]
	global_store_dwordx4 v[72:73], v[82:85], off
	v_or_b32_e32 v72, 32, v18
	v_ashrrev_i32_e32 v73, 31, v72
	s_cbranch_vccnz .LBB0_3497
	v_lshlrev_b64 v[74:75], s64, v[72:73]
	v_lshl_add_u64 v[74:75], v[74:75], 3, v[68:69]
	v_mov_b32_e32 v94, v173
	v_mov_b32_e32 v95, v141
	s_waitcnt vmcnt(4)
	v_mov_b64_e32 v[96:97], v[154:155]
	v_mov_b64_e32 v[98:99], v[156:157]
	v_mov_b64_e32 v[84:85], v[158:159]
	v_mov_b64_e32 v[86:87], v[160:161]
	v_mov_b64_e32 v[80:81], v[186:187]
	v_mov_b64_e32 v[82:83], v[188:189]
	v_mov_b64_e32 v[76:77], v[190:191]
	v_mov_b64_e32 v[78:79], v[192:193]
	v_pk_mul_f32 v[94:95], v[94:95], v[98:99]
	s_nop 0
	v_mov_b32_e32 v103, v94
	v_mov_b32_e32 v105, v95
	v_mov_b32_e32 v75, v78
	v_mov_b32_e32 v78, v77
	v_mov_b32_e32 v74, v76
	v_pk_mul_f32 v[90:91], v[142:143], v[78:79]
	v_pk_mul_f32 v[76:77], v[174:175], v[78:79]
	v_mov_b32_e32 v79, v82
	v_mov_b32_e32 v82, v81
	v_mov_b32_e32 v78, v80
	v_pk_mul_f32 v[92:93], v[144:145], v[82:83]
	v_pk_mul_f32 v[80:81], v[176:177], v[82:83]
	v_mov_b32_e32 v83, v86
	v_mov_b32_e32 v86, v85
	v_mov_b32_e32 v82, v84
	v_pk_mul_f32 v[100:101], v[138:139], v[86:87]
	v_pk_fma_f32 v[94:95], v[176:177], v[78:79], v[92:93] neg_lo:[0,0,1] neg_hi:[0,0,1]
	v_pk_fma_f32 v[92:93], v[170:171], v[82:83], v[100:101] neg_lo:[0,0,1] neg_hi:[0,0,1]
	v_mov_b32_e32 v100, v141
	v_mov_b32_e32 v101, v173
	v_pk_mul_f32 v[98:99], v[100:101], v[98:99]
	v_pk_mul_f32 v[84:85], v[170:171], v[86:87]
	v_mul_f32_e32 v102, v172, v96
	v_mul_f32_e32 v104, v140, v97
	v_mul_f32_e32 v86, v140, v96
	v_mul_f32_e32 v88, v172, v97
	v_mov_b32_e32 v87, v98
	v_mov_b32_e32 v89, v99
	v_pk_fma_f32 v[96:97], v[174:175], v[74:75], v[90:91] neg_lo:[0,0,1] neg_hi:[0,0,1]
	v_pk_add_f32 v[90:91], v[102:103], v[104:105] neg_lo:[0,1] neg_hi:[0,1]
	v_pk_fma_f32 v[98:99], v[142:143], v[74:75], v[76:77]
	v_pk_fma_f32 v[78:79], v[144:145], v[78:79], v[80:81]
	v_pk_fma_f32 v[76:77], v[138:139], v[82:83], v[84:85]
	v_pk_add_f32 v[74:75], v[86:87], v[88:89]
	s_and_b64 vcc, exec, s[6:7]
	s_mov_b64 s[60:61], -1
	v_add_u32_e32 v128, 0x80, v18
	v_ashrrev_i32_e32 v129, 31, v128
	v_lshlrev_b64 v[128:129], s64, v[128:129]
	v_lshl_add_u64 v[128:129], v[128:129], 3, v[68:69]
	global_load_dwordx4 v[106:109], v[128:129], off offset:48
	global_load_dwordx4 v[110:113], v[128:129], off offset:32
	global_load_dwordx4 v[114:117], v[128:129], off offset:16
	global_load_dwordx4 v[118:121], v[128:129], off
	s_cbranch_vccz .LBB0_3498
	s_branch .LBB0_3499

.LBB0_3501:
	v_pk_mul_f32 v[72:73], s[56:57], v[96:97]
	s_and_b64 vcc, exec, s[4:5]
	v_cvt_pk_bf16_f32 v82, v72, v73
	v_pk_mul_f32 v[72:73], s[56:57], v[94:95]
	s_nop 0
	v_cvt_pk_bf16_f32 v83, v72, v73
	v_pk_mul_f32 v[72:73], s[56:57], v[92:93]
	s_nop 0
	v_cvt_pk_bf16_f32 v84, v72, v73
	v_pk_mul_f32 v[72:73], s[56:57], v[90:91]
	s_nop 0
	v_cvt_pk_bf16_f32 v85, v72, v73
	v_pk_mul_f32 v[72:73], s[56:57], v[98:99]
	s_nop 0
	v_cvt_pk_bf16_f32 v86, v72, v73
	v_pk_mul_f32 v[72:73], s[56:57], v[78:79]
	s_nop 0
	v_cvt_pk_bf16_f32 v87, v72, v73
	v_pk_mul_f32 v[72:73], s[56:57], v[76:77]
	s_nop 0
	v_cvt_pk_bf16_f32 v88, v72, v73
	v_pk_mul_f32 v[72:73], s[56:57], v[74:75]
	s_nop 0
	v_cvt_pk_bf16_f32 v89, v72, v73
	v_lshl_add_u64 v[72:73], v[80:81], 1, s[54:55]
	global_store_dwordx4 v[72:73], v[82:85], off
	v_lshl_add_u64 v[72:73], v[72:73], 0, s[92:93]
	global_store_dwordx4 v[72:73], v[86:89], off
	v_or_b32_e32 v72, 48, v18
	v_ashrrev_i32_e32 v73, 31, v72
	s_cbranch_vccnz .LBB0_3503
	v_lshlrev_b64 v[74:75], s64, v[72:73]
	v_lshl_add_u64 v[74:75], v[74:75], 3, v[68:69]
	v_mov_b32_e32 v94, v165
	v_mov_b32_e32 v95, v133
	s_waitcnt vmcnt(4)
	v_mov_b64_e32 v[96:97], v[146:147]
	v_mov_b64_e32 v[98:99], v[148:149]
	v_mov_b64_e32 v[84:85], v[150:151]
	v_mov_b64_e32 v[86:87], v[152:153]
	v_mov_b64_e32 v[80:81], v[178:179]
	v_mov_b64_e32 v[82:83], v[180:181]
	v_mov_b64_e32 v[76:77], v[182:183]
	v_mov_b64_e32 v[78:79], v[184:185]
	v_pk_mul_f32 v[94:95], v[94:95], v[98:99]
	s_nop 0
	v_mov_b32_e32 v103, v94
	v_mov_b32_e32 v105, v95
	v_mov_b32_e32 v75, v78
	v_mov_b32_e32 v78, v77
	v_mov_b32_e32 v74, v76
	v_pk_mul_f32 v[90:91], v[134:135], v[78:79]
	v_pk_mul_f32 v[76:77], v[166:167], v[78:79]
	v_mov_b32_e32 v79, v82
	v_mov_b32_e32 v82, v81
	v_mov_b32_e32 v78, v80
	v_pk_mul_f32 v[92:93], v[136:137], v[82:83]
	v_pk_mul_f32 v[80:81], v[168:169], v[82:83]
	v_mov_b32_e32 v83, v86
	v_mov_b32_e32 v86, v85
	v_mov_b32_e32 v82, v84
	v_pk_mul_f32 v[100:101], v[130:131], v[86:87]
	v_pk_fma_f32 v[94:95], v[168:169], v[78:79], v[92:93] neg_lo:[0,0,1] neg_hi:[0,0,1]
	v_pk_fma_f32 v[92:93], v[162:163], v[82:83], v[100:101] neg_lo:[0,0,1] neg_hi:[0,0,1]
	v_mov_b32_e32 v100, v133
	v_mov_b32_e32 v101, v165
	v_pk_mul_f32 v[98:99], v[100:101], v[98:99]
	v_pk_mul_f32 v[84:85], v[162:163], v[86:87]
	v_mul_f32_e32 v102, v164, v96
	v_mul_f32_e32 v104, v132, v97
	v_mul_f32_e32 v86, v132, v96
	v_mul_f32_e32 v88, v164, v97
	v_mov_b32_e32 v87, v98
	v_mov_b32_e32 v89, v99
	v_pk_fma_f32 v[96:97], v[166:167], v[74:75], v[90:91] neg_lo:[0,0,1] neg_hi:[0,0,1]
	v_pk_add_f32 v[90:91], v[102:103], v[104:105] neg_lo:[0,1] neg_hi:[0,1]
	v_pk_fma_f32 v[98:99], v[134:135], v[74:75], v[76:77]
	v_pk_fma_f32 v[78:79], v[136:137], v[78:79], v[80:81]
	v_pk_fma_f32 v[76:77], v[130:131], v[82:83], v[84:85]
	v_pk_add_f32 v[74:75], v[86:87], v[88:89]
	s_and_b64 vcc, exec, s[6:7]
	s_mov_b64 s[60:61], -1
	v_add_u32_e32 v128, 0x90, v18
	v_ashrrev_i32_e32 v129, 31, v128
	v_lshlrev_b64 v[128:129], s64, v[128:129]
	v_lshl_add_u64 v[128:129], v[128:129], 3, v[68:69]
	global_load_dwordx4 v[154:157], v[128:129], off offset:48
	global_load_dwordx4 v[158:161], v[128:129], off offset:32
	global_load_dwordx4 v[186:189], v[128:129], off offset:16
	global_load_dwordx4 v[190:193], v[128:129], off
	s_cbranch_vccz .LBB0_3504
	s_branch .LBB0_3505

.LBB0_3507:
	v_pk_mul_f32 v[72:73], s[56:57], v[96:97]
	s_and_b64 vcc, exec, s[4:5]
	v_cvt_pk_bf16_f32 v82, v72, v73
	v_pk_mul_f32 v[72:73], s[56:57], v[94:95]
	s_nop 0
	v_cvt_pk_bf16_f32 v83, v72, v73
	v_pk_mul_f32 v[72:73], s[56:57], v[92:93]
	s_nop 0
	v_cvt_pk_bf16_f32 v84, v72, v73
	v_pk_mul_f32 v[72:73], s[56:57], v[90:91]
	s_nop 0
	v_cvt_pk_bf16_f32 v85, v72, v73
	v_pk_mul_f32 v[72:73], s[56:57], v[98:99]
	s_nop 0
	v_cvt_pk_bf16_f32 v86, v72, v73
	v_pk_mul_f32 v[72:73], s[56:57], v[78:79]
	s_nop 0
	v_cvt_pk_bf16_f32 v87, v72, v73
	v_pk_mul_f32 v[72:73], s[56:57], v[76:77]
	s_nop 0
	v_cvt_pk_bf16_f32 v88, v72, v73
	v_pk_mul_f32 v[72:73], s[56:57], v[74:75]
	s_nop 0
	v_cvt_pk_bf16_f32 v89, v72, v73
	v_lshl_add_u64 v[72:73], v[80:81], 1, s[54:55]
	global_store_dwordx4 v[72:73], v[82:85], off
	v_lshl_add_u64 v[72:73], v[72:73], 0, s[92:93]
	global_store_dwordx4 v[72:73], v[86:89], off
	v_add_u32_e32 v72, 0x80, v18
	v_ashrrev_i32_e32 v73, 31, v72
	s_cbranch_vccnz .LBB0_3509
	v_lshlrev_b64 v[74:75], s64, v[72:73]
	v_lshl_add_u64 v[74:75], v[74:75], 3, v[68:69]
	v_mov_b32_e32 v94, v57
	v_mov_b32_e32 v95, v53
	s_waitcnt vmcnt(4)
	v_mov_b64_e32 v[96:97], v[106:107]
	v_mov_b64_e32 v[98:99], v[108:109]
	v_mov_b64_e32 v[84:85], v[110:111]
	v_mov_b64_e32 v[86:87], v[112:113]
	v_mov_b64_e32 v[80:81], v[114:115]
	v_mov_b64_e32 v[82:83], v[116:117]
	v_mov_b64_e32 v[76:77], v[118:119]
	v_mov_b64_e32 v[78:79], v[120:121]
	v_pk_mul_f32 v[94:95], v[94:95], v[98:99]
	v_mul_f32_e32 v100, v56, v96
	v_mul_f32_e32 v102, v52, v97
	v_mov_b32_e32 v75, v78
	v_mov_b32_e32 v78, v77
	v_mov_b32_e32 v74, v76
	v_pk_mul_f32 v[88:89], v[62:63], v[78:79]
	v_pk_mul_f32 v[76:77], v[126:127], v[78:79]
	v_mov_b32_e32 v79, v82
	v_mov_b32_e32 v82, v81
	v_mov_b32_e32 v78, v80
	v_pk_mul_f32 v[90:91], v[54:55], v[82:83]
	v_pk_mul_f32 v[80:81], v[60:61], v[82:83]
	v_mov_b32_e32 v83, v86
	v_mov_b32_e32 v86, v85
	v_mov_b32_e32 v82, v84
	v_pk_mul_f32 v[84:85], v[58:59], v[86:87]
	v_mov_b32_e32 v101, v94
	v_mov_b32_e32 v103, v95
	v_pk_fma_f32 v[94:95], v[126:127], v[74:75], v[88:89] neg_lo:[0,0,1] neg_hi:[0,0,1]
	v_pk_fma_f32 v[88:89], v[64:65], v[82:83], v[84:85] neg_lo:[0,0,1] neg_hi:[0,0,1]
	v_pk_add_f32 v[84:85], v[100:101], v[102:103] neg_lo:[0,1] neg_hi:[0,1]
	v_mov_b32_e32 v100, v53
	v_mov_b32_e32 v101, v57
	v_pk_mul_f32 v[98:99], v[100:101], v[98:99]
	v_pk_mul_f32 v[86:87], v[64:65], v[86:87]
	v_mul_f32_e32 v92, v52, v96
	v_mul_f32_e32 v96, v56, v97
	v_mov_b32_e32 v93, v98
	v_mov_b32_e32 v97, v99
	v_pk_fma_f32 v[90:91], v[60:61], v[78:79], v[90:91] neg_lo:[0,0,1] neg_hi:[0,0,1]
	v_pk_fma_f32 v[98:99], v[62:63], v[74:75], v[76:77]
	v_pk_fma_f32 v[78:79], v[54:55], v[78:79], v[80:81]
	v_pk_fma_f32 v[76:77], v[58:59], v[82:83], v[86:87]
	v_pk_add_f32 v[74:75], v[92:93], v[96:97]
	s_and_b64 vcc, exec, s[6:7]
	s_mov_b64 s[60:61], -1
	v_add_u32_e32 v128, 0xa0, v18
	v_ashrrev_i32_e32 v129, 31, v128
	v_lshlrev_b64 v[128:129], s64, v[128:129]
	v_lshl_add_u64 v[128:129], v[128:129], 3, v[68:69]
	global_load_dwordx4 v[146:149], v[128:129], off offset:48
	global_load_dwordx4 v[150:153], v[128:129], off offset:32
	global_load_dwordx4 v[178:181], v[128:129], off offset:16
	global_load_dwordx4 v[182:185], v[128:129], off
	s_cbranch_vccz .LBB0_3510
	s_branch .LBB0_3511

.LBB0_3513:
	v_pk_mul_f32 v[72:73], s[56:57], v[94:95]
	s_and_b64 vcc, exec, s[4:5]
	v_cvt_pk_bf16_f32 v86, v72, v73
	v_pk_mul_f32 v[72:73], s[56:57], v[90:91]
	s_mov_b32 s65, 0x800000
	v_cvt_pk_bf16_f32 v87, v72, v73
	v_pk_mul_f32 v[72:73], s[56:57], v[88:89]
	s_nop 0
	v_cvt_pk_bf16_f32 v88, v72, v73
	v_pk_mul_f32 v[72:73], s[56:57], v[84:85]
	s_nop 0
	v_cvt_pk_bf16_f32 v89, v72, v73
	v_pk_mul_f32 v[72:73], s[56:57], v[98:99]
	s_nop 0
	v_cvt_pk_bf16_f32 v82, v72, v73
	v_pk_mul_f32 v[72:73], s[56:57], v[78:79]
	s_nop 0
	v_cvt_pk_bf16_f32 v83, v72, v73
	v_pk_mul_f32 v[72:73], s[56:57], v[76:77]
	s_nop 0
	v_cvt_pk_bf16_f32 v84, v72, v73
	v_pk_mul_f32 v[72:73], s[56:57], v[74:75]
	s_nop 0
	v_cvt_pk_bf16_f32 v85, v72, v73
	v_lshl_add_u64 v[72:73], v[80:81], 1, s[54:55]
	global_store_dwordx4 v[72:73], v[86:89], off
	v_lshl_add_u64 v[72:73], v[72:73], 0, s[92:93]
	global_store_dwordx4 v[72:73], v[82:85], off
	v_add_u32_e32 v72, 0x90, v18
	v_ashrrev_i32_e32 v73, 31, v72
	s_cbranch_vccnz .LBB0_3515
	v_lshlrev_b64 v[74:75], s64, v[72:73]
	v_lshl_add_u64 v[74:75], v[74:75], 3, v[68:69]
	v_mov_b32_e32 v94, v41
	v_mov_b32_e32 v95, v37
	s_waitcnt vmcnt(4)
	v_mov_b64_e32 v[96:97], v[154:155]
	v_mov_b64_e32 v[98:99], v[156:157]
	v_mov_b64_e32 v[84:85], v[158:159]
	v_mov_b64_e32 v[86:87], v[160:161]
	v_mov_b64_e32 v[80:81], v[186:187]
	v_mov_b64_e32 v[82:83], v[188:189]
	v_mov_b64_e32 v[76:77], v[190:191]
	v_mov_b64_e32 v[78:79], v[192:193]
	v_pk_mul_f32 v[94:95], v[94:95], v[98:99]
	s_nop 0
	v_mov_b32_e32 v103, v94
	v_mov_b32_e32 v105, v95
	v_mov_b32_e32 v75, v78
	v_mov_b32_e32 v78, v77
	v_mov_b32_e32 v74, v76
	v_pk_mul_f32 v[90:91], v[46:47], v[78:79]
	v_pk_mul_f32 v[76:77], v[50:51], v[78:79]
	v_mov_b32_e32 v79, v82
	v_mov_b32_e32 v82, v81
	v_mov_b32_e32 v78, v80
	v_pk_mul_f32 v[92:93], v[38:39], v[82:83]
	v_pk_mul_f32 v[80:81], v[44:45], v[82:83]
	v_mov_b32_e32 v83, v86
	v_mov_b32_e32 v86, v85
	v_mov_b32_e32 v82, v84
	v_pk_mul_f32 v[100:101], v[42:43], v[86:87]
	v_pk_fma_f32 v[94:95], v[44:45], v[78:79], v[92:93] neg_lo:[0,0,1] neg_hi:[0,0,1]
	v_pk_fma_f32 v[92:93], v[48:49], v[82:83], v[100:101] neg_lo:[0,0,1] neg_hi:[0,0,1]
	v_mov_b32_e32 v100, v37
	v_mov_b32_e32 v101, v41
	v_pk_mul_f32 v[98:99], v[100:101], v[98:99]
	v_pk_mul_f32 v[84:85], v[48:49], v[86:87]
	v_mul_f32_e32 v102, v40, v96
	v_mul_f32_e32 v104, v36, v97
	v_mul_f32_e32 v86, v36, v96
	v_mul_f32_e32 v88, v40, v97
	v_mov_b32_e32 v87, v98
	v_mov_b32_e32 v89, v99
	v_pk_fma_f32 v[96:97], v[50:51], v[74:75], v[90:91] neg_lo:[0,0,1] neg_hi:[0,0,1]
	v_pk_add_f32 v[90:91], v[102:103], v[104:105] neg_lo:[0,1] neg_hi:[0,1]
	v_pk_fma_f32 v[98:99], v[46:47], v[74:75], v[76:77]
	v_pk_fma_f32 v[78:79], v[38:39], v[78:79], v[80:81]
	v_pk_fma_f32 v[76:77], v[42:43], v[82:83], v[84:85]
	v_pk_add_f32 v[74:75], v[86:87], v[88:89]
	s_and_b64 vcc, exec, s[6:7]
	s_mov_b64 s[60:61], -1
	v_add_u32_e32 v128, 0xb0, v18
	v_ashrrev_i32_e32 v129, 31, v128
	v_lshlrev_b64 v[128:129], s64, v[128:129]
	v_lshl_add_u64 v[128:129], v[128:129], 3, v[68:69]
	global_load_dwordx4 v[106:109], v[128:129], off offset:48
	global_load_dwordx4 v[110:113], v[128:129], off offset:32
	global_load_dwordx4 v[114:117], v[128:129], off offset:16
	global_load_dwordx4 v[118:121], v[128:129], off
	s_cbranch_vccz .LBB0_3516
	s_branch .LBB0_3517

.LBB0_3519:
	v_pk_mul_f32 v[72:73], s[56:57], v[96:97]
	s_and_b64 vcc, exec, s[4:5]
	v_cvt_pk_bf16_f32 v82, v72, v73
	v_pk_mul_f32 v[72:73], s[56:57], v[94:95]
	s_nop 0
	v_cvt_pk_bf16_f32 v83, v72, v73
	v_pk_mul_f32 v[72:73], s[56:57], v[92:93]
	s_nop 0
	v_cvt_pk_bf16_f32 v84, v72, v73
	v_pk_mul_f32 v[72:73], s[56:57], v[90:91]
	s_nop 0
	v_cvt_pk_bf16_f32 v85, v72, v73
	v_pk_mul_f32 v[72:73], s[56:57], v[98:99]
	s_nop 0
	v_cvt_pk_bf16_f32 v86, v72, v73
	v_pk_mul_f32 v[72:73], s[56:57], v[78:79]
	s_nop 0
	v_cvt_pk_bf16_f32 v87, v72, v73
	v_pk_mul_f32 v[72:73], s[56:57], v[76:77]
	s_nop 0
	v_cvt_pk_bf16_f32 v88, v72, v73
	v_pk_mul_f32 v[72:73], s[56:57], v[74:75]
	s_nop 0
	v_cvt_pk_bf16_f32 v89, v72, v73
	v_lshl_add_u64 v[72:73], v[80:81], 1, s[54:55]
	global_store_dwordx4 v[72:73], v[82:85], off
	v_lshl_add_u64 v[72:73], v[72:73], 0, s[92:93]
	global_store_dwordx4 v[72:73], v[86:89], off
	v_add_u32_e32 v72, 0xa0, v18
	v_ashrrev_i32_e32 v73, 31, v72
	s_cbranch_vccnz .LBB0_3521
	v_lshlrev_b64 v[74:75], s64, v[72:73]
	v_lshl_add_u64 v[74:75], v[74:75], 3, v[68:69]
	v_mov_b32_e32 v94, v25
	v_mov_b32_e32 v95, v21
	s_waitcnt vmcnt(4)
	v_mov_b64_e32 v[96:97], v[146:147]
	v_mov_b64_e32 v[98:99], v[148:149]
	v_mov_b64_e32 v[84:85], v[150:151]
	v_mov_b64_e32 v[86:87], v[152:153]
	v_mov_b64_e32 v[80:81], v[178:179]
	v_mov_b64_e32 v[82:83], v[180:181]
	v_mov_b64_e32 v[76:77], v[182:183]
	v_mov_b64_e32 v[78:79], v[184:185]
	v_pk_mul_f32 v[94:95], v[94:95], v[98:99]
	s_nop 0
	v_mov_b32_e32 v103, v94
	v_mov_b32_e32 v105, v95
	v_mov_b32_e32 v75, v78
	v_mov_b32_e32 v78, v77
	v_mov_b32_e32 v74, v76
	v_pk_mul_f32 v[90:91], v[30:31], v[78:79]
	v_pk_mul_f32 v[76:77], v[34:35], v[78:79]
	v_mov_b32_e32 v79, v82
	v_mov_b32_e32 v82, v81
	v_mov_b32_e32 v78, v80
	v_pk_mul_f32 v[92:93], v[22:23], v[82:83]
	v_pk_mul_f32 v[80:81], v[28:29], v[82:83]
	v_mov_b32_e32 v83, v86
	v_mov_b32_e32 v86, v85
	v_mov_b32_e32 v82, v84
	v_pk_mul_f32 v[100:101], v[26:27], v[86:87]
	v_pk_fma_f32 v[94:95], v[28:29], v[78:79], v[92:93] neg_lo:[0,0,1] neg_hi:[0,0,1]
	v_pk_fma_f32 v[92:93], v[32:33], v[82:83], v[100:101] neg_lo:[0,0,1] neg_hi:[0,0,1]
	v_mov_b32_e32 v100, v21
	v_mov_b32_e32 v101, v25
	v_pk_mul_f32 v[98:99], v[100:101], v[98:99]
	v_pk_mul_f32 v[84:85], v[32:33], v[86:87]
	v_mul_f32_e32 v102, v24, v96
	v_mul_f32_e32 v104, v20, v97
	v_mul_f32_e32 v86, v20, v96
	v_mul_f32_e32 v88, v24, v97
	v_mov_b32_e32 v87, v98
	v_mov_b32_e32 v89, v99
	v_pk_fma_f32 v[96:97], v[34:35], v[74:75], v[90:91] neg_lo:[0,0,1] neg_hi:[0,0,1]
	v_pk_add_f32 v[90:91], v[102:103], v[104:105] neg_lo:[0,1] neg_hi:[0,1]
	v_pk_fma_f32 v[98:99], v[30:31], v[74:75], v[76:77]
	v_pk_fma_f32 v[78:79], v[22:23], v[78:79], v[80:81]
	v_pk_fma_f32 v[76:77], v[26:27], v[82:83], v[84:85]
	v_pk_add_f32 v[74:75], v[86:87], v[88:89]
	s_and_b64 vcc, exec, s[6:7]
	s_mov_b64 s[60:61], -1
	s_cbranch_vccz .LBB0_3522
	s_branch .LBB0_3523

.LBB0_3525:
	v_pk_mul_f32 v[72:73], s[56:57], v[96:97]
	s_and_b64 vcc, exec, s[4:5]
	v_cvt_pk_bf16_f32 v82, v72, v73
	v_pk_mul_f32 v[72:73], s[56:57], v[94:95]
	s_mov_b64 s[60:61], 0x400
	v_cvt_pk_bf16_f32 v83, v72, v73
	v_pk_mul_f32 v[72:73], s[56:57], v[92:93]
	s_nop 0
	v_cvt_pk_bf16_f32 v84, v72, v73
	v_pk_mul_f32 v[72:73], s[56:57], v[90:91]
	s_nop 0
	v_cvt_pk_bf16_f32 v85, v72, v73
	v_pk_mul_f32 v[72:73], s[56:57], v[98:99]
	s_nop 0
	v_cvt_pk_bf16_f32 v86, v72, v73
	v_pk_mul_f32 v[72:73], s[56:57], v[78:79]
	s_nop 0
	v_cvt_pk_bf16_f32 v87, v72, v73
	v_pk_mul_f32 v[72:73], s[56:57], v[76:77]
	s_nop 0
	v_cvt_pk_bf16_f32 v88, v72, v73
	v_pk_mul_f32 v[72:73], s[56:57], v[74:75]
	s_nop 0
	v_cvt_pk_bf16_f32 v89, v72, v73
	v_lshl_add_u64 v[72:73], v[80:81], 1, s[54:55]
	global_store_dwordx4 v[72:73], v[82:85], off
	v_lshl_add_u64 v[72:73], v[72:73], 0, s[92:93]
	global_store_dwordx4 v[72:73], v[86:89], off
	v_add_u32_e32 v72, 0xb0, v18
	v_ashrrev_i32_e32 v73, 31, v72
	s_cbranch_vccnz .LBB0_3527
	v_lshlrev_b64 v[74:75], s64, v[72:73]
	v_lshl_add_u64 v[68:69], v[74:75], 3, v[68:69]
	s_waitcnt vmcnt(0)
	v_mov_b64_e32 v[94:95], v[106:107]
	v_mov_b64_e32 v[96:97], v[108:109]
	v_mov_b64_e32 v[82:83], v[110:111]
	v_mov_b64_e32 v[84:85], v[112:113]
	v_mov_b64_e32 v[78:79], v[114:115]
	v_mov_b64_e32 v[80:81], v[116:117]
	v_mov_b64_e32 v[74:75], v[118:119]
	v_mov_b64_e32 v[76:77], v[120:121]
	v_mul_f32_e32 v100, v2, v95
	v_mul_f32_e32 v86, v2, v94
	v_mul_f32_e32 v90, v6, v95
	v_mov_b32_e32 v69, v76
	v_mov_b32_e32 v76, v75
	v_mov_b32_e32 v68, v74
	v_pk_mul_f32 v[88:89], v[12:13], v[76:77]
	v_pk_mul_f32 v[74:75], v[16:17], v[76:77]
	v_mov_b32_e32 v77, v80
	v_mov_b32_e32 v80, v79
	v_mov_b32_e32 v76, v78
	v_pk_mul_f32 v[92:93], v[4:5], v[80:81]
	v_pk_mul_f32 v[78:79], v[10:11], v[80:81]
	v_mov_b32_e32 v81, v84
	v_mov_b32_e32 v84, v83
	v_mov_b32_e32 v80, v82
	v_pk_mul_f32 v[98:99], v[8:9], v[84:85]
	v_pk_mul_f32 v[82:83], v[14:15], v[84:85]
	v_mul_f32_e32 v84, v6, v94
	v_mov_b32_e32 v94, v7
	v_mov_b32_e32 v95, v3
	v_pk_mul_f32 v[94:95], v[94:95], v[96:97]
	v_pk_fma_f32 v[92:93], v[10:11], v[76:77], v[92:93] neg_lo:[0,0,1] neg_hi:[0,0,1]
	v_mov_b32_e32 v85, v94
	v_mov_b32_e32 v101, v95
	v_pk_fma_f32 v[94:95], v[16:17], v[68:69], v[88:89] neg_lo:[0,0,1] neg_hi:[0,0,1]
	v_pk_fma_f32 v[88:89], v[14:15], v[80:81], v[98:99] neg_lo:[0,0,1] neg_hi:[0,0,1]
	v_mov_b32_e32 v98, v3
	v_mov_b32_e32 v99, v7
	v_pk_mul_f32 v[96:97], v[98:99], v[96:97]
	v_pk_add_f32 v[84:85], v[84:85], v[100:101] neg_lo:[0,1] neg_hi:[0,1]
	v_mov_b32_e32 v87, v96
	v_mov_b32_e32 v91, v97
	v_pk_fma_f32 v[96:97], v[12:13], v[68:69], v[74:75]
	v_pk_fma_f32 v[76:77], v[4:5], v[76:77], v[78:79]
	v_pk_fma_f32 v[74:75], v[8:9], v[80:81], v[82:83]
	v_pk_add_f32 v[68:69], v[86:87], v[90:91]
	s_movk_i32 s64, 0x1800
	s_and_b64 vcc, exec, s[6:7]
	s_mov_b64 s[4:5], -1
	s_cbranch_vccnz .LBB0_3529
	s_branch .LBB0_3528
